# speedup vs baseline: 1.0433x; 1.0046x over previous
_Z11main_kernelPKhPKfPf:
	s_load_dwordx4 s[12:15], s[0:1], 0x0
	s_load_dwordx2 s[10:11], s[0:1], 0x10
	s_bfe_u32 s4, s2, 0x50003
	s_sub_u32 s61, s4, 24
	s_cmp_lt_u32 s61, 4
	s_cselect_b32 s61, 1, 0
	s_lshl_b32 s62, s61, 2
	s_add_u32 s4, s4, s62
	s_cmp_gt_u32 s4, 27
	s_cselect_b64 s[16:17], -1, 0
	s_cmp_lt_u32 s4, 28
	v_readfirstlane_b32 s21, v0
	s_cselect_b64 s[6:7], -1, 0
	s_mov_b32 s28, 0
	s_and_b64 vcc, exec, s[16:17]
	s_mov_b32 s42, 0
	s_cbranch_vccnz .LBB1_6
	s_mov_b32 s1, 0
	s_cmp_lt_u32 s4, 7
	s_mov_b32 s0, s4
	s_cbranch_scc1 .LBB1_5
	s_mov_b32 s5, -8
	s_mov_b32 s1, 6
	s_mov_b32 s0, s4

.LBB1_6:
	s_lshr_b32 s5, s2, 3
	s_add_i32 s0, s5, 4
	s_and_b32 s8, s0, 31
	s_sub_u32 s8, s8, s62
	s_cmp_gt_u32 s8, 27
	s_cselect_b64 s[18:19], -1, 0
	s_cmp_lt_u32 s8, 28
	s_cselect_b64 s[0:1], -1, 0
	s_mov_b32 s29, 0
	s_and_b64 vcc, exec, s[18:19]
	s_mov_b32 s43, 0
	s_cbranch_vccnz .LBB1_12
	s_cmp_lt_u32 s8, 7
	s_mov_b32 s3, s8
	s_cbranch_scc1 .LBB1_11
	s_mov_b32 s22, -8
	s_mov_b32 s9, 6
	s_mov_b32 s3, s8

.LBB1_12:
	s_lshl_b32 s2, s2, 6
	s_and_b32 s9, s2, 0x1c0
	s_lshr_b32 s2, s9, 5
	s_lshr_b32 s3, s21, 6
	v_bfe_u32 v22, v0, 5, 1
	s_or_b32 s33, s2, 1
	s_xor_b32 s33, s33, s61
	s_lshl_b32 s2, s3, 5
	v_lshlrev_b32_e32 v1, 2, v22
	v_or_b32_e32 v18, s2, v1
	v_mov_b32_e32 v19, 0
	s_waitcnt lgkmcnt(0)
	v_lshl_add_u64 v[2:3], v[18:19], 2, s[12:13]
	s_mov_b64 s[22:23], 0x424000
	v_and_b32_e32 v199, 63, v0
	v_lshl_add_u64 v[20:21], v[2:3], 0, s[22:23]
	v_add_co_u32_e32 v24, vcc, 0x424000, v2
	s_add_u32 s22, s12, 0x420000
	s_nop 0
	v_addc_co_u32_e32 v25, vcc, 0, v3, vcc
	global_load_dwordx4 v[6:9], v[20:21], off offset:32
	global_load_dwordx4 v[10:13], v[20:21], off offset:64
	global_load_dwordx4 v[2:5], v[24:25], off
	global_load_dwordx4 v[14:17], v[20:21], off offset:96
	s_addc_u32 s23, s13, 0
	v_lshl_or_b32 v18, s3, 7, v199
	v_lshl_add_u64 v[20:21], v[18:19], 4, s[22:23]
	v_ashrrev_i32_e32 v19, 31, v18
	v_lshl_add_u64 v[18:19], v[18:19], 4, s[22:23]
	global_load_dwordx4 v[70:73], v[20:21], off
	global_load_dwordx4 v[66:69], v[18:19], off offset:1024
	s_lshl_b32 s20, s33, 7
	s_and_b64 vcc, exec, s[0:1]
	s_cbranch_vccz .LBB1_14
	s_lshl_b32 s0, s29, 4
	s_add_i32 s30, s0, s20
	s_sub_i32 s38, s8, 28
	s_mov_b32 s44, 64
	s_cbranch_execz .LBB1_15
	s_branch .LBB1_16

.LBB1_16:
	s_add_i32 s9, s9, s5
	s_lshr_b32 s39, s9, 5
	s_xor_b32 s39, s39, s61
	s_sub_i32 s40, s4, 28
	s_lshl_b32 s4, s39, 7
	s_and_b64 vcc, exec, s[6:7]
	s_cbranch_vccz .LBB1_18
	s_add_i32 s9, s28, s4
	s_lshl_b32 s8, s40, 5
	s_mov_b32 s20, 64
	s_cbranch_execz .LBB1_19
	s_branch .LBB1_20

.LBB1_235:
	v_subrev_u32_e32 v0, 0x100, v0
	s_movk_i32 s0, 0xf0
	v_cmp_gt_u32_e32 vcc, s0, v0
	s_and_saveexec_b64 s[0:1], vcc
	s_cbranch_execz .Lepi_idle
	s_movk_i32 s0, 0x77
	v_mov_b32_e32 v1, 0xffffff88
	v_cmp_lt_u32_e32 vcc, s0, v0
	v_mov_b32_e32 v2, 0x44704000
	s_mov_b32 s0, 0xf800000
	v_cndmask_b32_e32 v1, 0, v1, vcc
	v_add_u32_e32 v0, v1, v0
	v_cvt_f32_u32_e32 v1, v0
	s_mov_b32 s5, 0x17800
	s_mov_b32 s4, 0x3eb17218
	v_fmac_f32_e32 v2, 0xc1000000, v1
	v_mul_f32_e32 v1, 0x4f800000, v2
	v_cmp_gt_f32_e64 s[0:1], s0, v2
	s_nop 1
	v_cndmask_b32_e64 v1, v2, v1, s[0:1]
	v_sqrt_f32_e32 v2, v1
	s_nop 0
	v_add_u32_e32 v3, -1, v2
	v_fma_f32 v4, -v3, v2, v1
	v_cmp_ge_f32_e64 s[2:3], 0, v4
	v_add_u32_e32 v4, 1, v2
	s_nop 0
	v_cndmask_b32_e64 v3, v2, v3, s[2:3]
	v_fma_f32 v2, -v4, v2, v1
	v_cmp_lt_f32_e64 s[2:3], 0, v2
	s_nop 1
	v_cndmask_b32_e64 v2, v3, v4, s[2:3]
	v_mul_f32_e32 v3, 0x37800000, v2
	v_cndmask_b32_e64 v2, v2, v3, s[0:1]
	v_mov_b32_e32 v3, 0x260
	v_cmp_class_f32_e64 s[0:1], v1, v3
	s_nop 1
	v_cndmask_b32_e64 v1, v2, v1, s[0:1]
	v_sub_f32_e32 v1, 0x41f80000, v1
	v_mul_f32_e32 v1, 0.5, v1
	v_cvt_i32_f32_e32 v1, v1
	s_and_b64 s[0:1], exec, s[16:17]
	s_cselect_b32 s2, s40, s38
	s_cselect_b32 s3, s39, s33
	v_sub_u32_e32 v2, 31, v1
	v_mul_lo_u32 v2, v2, v1
	v_lshrrev_b32_e32 v3, 31, v2
	v_add_u32_e32 v2, v2, v3
	v_ashrrev_i32_e32 v2, 1, v2
	v_cmp_gt_i32_e64 s[0:1], v2, v0
	s_nop 1
	v_subbrev_co_u32_e64 v1, s[0:1], 0, v1, s[0:1]
	v_add_u32_e32 v2, 1, v1
	v_sub_u32_e32 v3, 30, v1
	v_mul_lo_u32 v3, v2, v3
	v_lshrrev_b32_e32 v4, 31, v3
	v_add_u32_e32 v3, v3, v4
	v_ashrrev_i32_e32 v3, 1, v3
	v_cmp_gt_i32_e64 s[0:1], v3, v0
	s_nop 1
	v_cndmask_b32_e64 v12, v2, v1, s[0:1]
	v_sub_u32_e32 v1, 31, v12
	v_mul_lo_u32 v1, v1, v12
	v_lshrrev_b32_e32 v2, 31, v1
	v_add_u32_e32 v1, v1, v2
	v_ashrrev_i32_e32 v1, 1, v1
	v_sub_u32_e32 v0, v0, v1
	v_cndmask_b32_e64 v1, 0, 16, vcc
	v_lshl_or_b32 v1, s2, 5, v1
	v_add_u32_e32 v1, v1, v12
	v_sub_u32_e32 v2, 0xff, v1
	v_mul_lo_u32 v1, v2, v1
	v_lshrrev_b32_e32 v2, 31, v1
	v_add_u32_e32 v1, v1, v2
	v_ashrrev_i32_e32 v1, 1, v1
	v_add3_u32 v13, v12, v0, 1
	v_add_u32_e32 v0, v1, v0
	v_ashrrev_i32_e32 v1, 31, v0
	v_mov_b32_e32 v2, 0x1fc0
	v_mad_u64_u32 v[0:1], s[0:1], s3, v2, v[0:1]
	v_mad_u64_u32 v[4:5], s[0:1], v0, 24, s[10:11]
	v_mov_b32_e32 v0, 0x17800
	v_lshl_add_u32 v14, v12, 2, v0
	v_mov_b32_e32 v0, 0x60
	v_cndmask_b32_e32 v15, 0, v0, vcc
	v_or_b32_e32 v2, 16, v15
	v_add_lshl_u32 v3, v2, v12, 6
	v_add_u32_e32 v2, v2, v13
	v_lshl_add_u32 v6, v2, 6, v14
	v_add_u32_e32 v2, 32, v15
	v_add_lshl_u32 v7, v2, v12, 6
	v_add_u32_e32 v2, v2, v13
	v_lshl_add_u32 v8, v2, 6, v14
	v_add_u32_e32 v2, 48, v15
	v_mad_i32_i24 v5, v1, 24, v5
	v_add_lshl_u32 v0, v15, v12, 6
	v_lshlrev_b32_e32 v16, 2, v13
	v_add_u32_e32 v1, v15, v13
	v_add_lshl_u32 v9, v2, v12, 6
	v_add_u32_e32 v17, 64, v15
	v_add_u32_e32 v15, 0x50, v15
	v_add3_u32 v0, v0, v16, s5
	v_lshl_add_u32 v1, v1, 6, v14
	v_add3_u32 v3, v3, v16, s5
	v_add3_u32 v7, v7, v16, s5
	v_add3_u32 v9, v9, v16, s5
	v_add_u32_e32 v2, v2, v13
	v_add_lshl_u32 v18, v17, v12, 6
	v_add_lshl_u32 v12, v15, v12, 6
	s_load_dwordx4 s[0:3], s[14:15], 0x0
	v_lshl_add_u32 v10, v2, 6, v14
	ds_read_b32 v0, v0
	ds_read_b32 v2, v1
	ds_read_b32 v1, v3
	ds_read_b32 v3, v6
	ds_read_b32 v6, v7
	ds_read_b32 v8, v8
	ds_read_b32 v7, v9
	ds_read_b32 v9, v10
	v_add3_u32 v18, v18, v16, s5
	v_add3_u32 v16, v12, v16, s5
	v_add_u32_e32 v12, v15, v13
	v_add_u32_e32 v17, v17, v13
	v_lshl_add_u32 v15, v12, 6, v14
	s_load_dwordx2 s[6:7], s[14:15], 0x10
	v_lshl_add_u32 v17, v17, 6, v14
	ds_read_b32 v12, v18
	ds_read_b32 v14, v17
	ds_read_b32 v13, v16
	ds_read_b32 v15, v15
	s_waitcnt lgkmcnt(0)
	v_pk_add_f32 v[0:1], v[0:1], v[2:3]
	v_mov_b32_e32 v2, s2
	v_mov_b32_e32 v3, s3
	v_mov_b64_e32 v[10:11], s[0:1]
	v_pk_add_f32 v[6:7], v[6:7], v[8:9]
	v_pk_fma_f32 v[0:1], v[0:1], s[4:5], v[10:11] op_sel_hi:[1,0,1]
	v_pk_fma_f32 v[2:3], v[6:7], s[4:5], v[2:3] op_sel_hi:[1,0,1]
	global_store_dwordx4 v[4:5], v[0:3], off
	s_nop 1
	v_pk_add_f32 v[0:1], v[12:13], v[14:15]
	v_mov_b64_e32 v[2:3], s[6:7]
	v_pk_fma_f32 v[0:1], v[0:1], s[4:5], v[2:3] op_sel_hi:[1,0,1]
	global_store_dwordx2 v[4:5], v[0:1], off offset:16
	s_endpgm
.Lepi_idle:
	s_endpgm
.LBB1_237:
.LBB1_238:
	s_and_saveexec_b64 s[0:1], s[4:5]
	s_cbranch_execz .LBB1_240
	ds_read2_b32 v[2:3], v180 offset1:224
	v_add_u32_e32 v1, 0x700, v180
	ds_read2_b32 v[4:5], v1 offset1:224
	ds_read_b32 v6, v187
	ds_read_b32 v7, v188
	ds_read_b32 v8, v185
	ds_read_b32 v9, v186
	ds_read_b32 v10, v183
	ds_read_b32 v11, v184
	ds_read_b32 v12, v181
	ds_read_b32 v13, v182
	s_sub_i32 s2, 0x78, s30
	s_mul_i32 s2, s2, 6
	s_waitcnt lgkmcnt(6)
	v_pk_add_f32 v[2:3], v[2:3], v[6:7]
	s_ashr_i32 s3, s2, 31
	v_add_f32_e32 v1, 0, v2
	v_add_f32_e32 v1, v1, v3
	s_waitcnt lgkmcnt(4)
	v_pk_add_f32 v[2:3], v[4:5], v[8:9]
	v_add_u32_e32 v4, 0xe00, v180
	ds_read2_b32 v[4:5], v4 offset1:224
	v_add_f32_e32 v1, v1, v2
	v_add_u32_e32 v2, 0x1500, v180
	ds_read2_b32 v[6:7], v2 offset1:224
	v_add_f32_e32 v1, v1, v3
	s_waitcnt lgkmcnt(1)
	v_pk_add_f32 v[2:3], v[4:5], v[10:11]
	s_lshl_b64 s[4:5], s[12:13], 2
	v_add_f32_e32 v1, v1, v2
	v_add_f32_e32 v1, v1, v3
	s_waitcnt lgkmcnt(0)
	v_pk_add_f32 v[2:3], v[6:7], v[12:13]
	s_add_u32 s4, s10, s4
	v_add_f32_e32 v1, v1, v2
	s_addc_u32 s5, s11, s5
	s_lshl_b64 s[2:3], s[2:3], 2
	v_add_f32_e32 v1, v1, v3
	s_add_u32 s2, s4, s2
	v_fmamk_f32 v1, v1, 0x3eb17218, v176
	s_addc_u32 s3, s5, s3
	v_lshlrev_b32 v2, 2, v0
	global_store_dword v2, v1, s[2:3]
